# lora pass: weight fragment loads of K-trip t+1 prefetched before trip t's MFMAs
# speedup vs baseline: 1.0098x; 1.0051x over previous
.LBB0_1717:
	v_or_b32_e32 v44, s4, v59
	s_waitcnt vmcnt(8)
	v_lshlrev_b64 v[10:11], s17, v[44:45]
	v_or_b32_e32 v44, 16, v44
	v_mov_b32_e32 v38, 0
	s_xor_b64 s[26:27], s[0:1], -1
	v_lshlrev_b64 v[12:13], s17, v[44:45]
	v_mov_b32_e32 v30, v92
	s_mov_b32 s6, s33
	s_mov_b32 s0, s15
	v_mov_b32_e32 v39, v38
	v_mov_b32_e32 v40, v38
	v_mov_b32_e32 v41, v38
	v_mov_b32_e32 v18, v38
	v_mov_b32_e32 v19, v38
	v_mov_b32_e32 v20, v38
	v_mov_b32_e32 v21, v38
	v_mov_b32_e32 v34, v38
	v_mov_b32_e32 v35, v38
	v_mov_b32_e32 v36, v38
	v_mov_b32_e32 v37, v38
	v_mov_b32_e32 v14, v38
	v_mov_b32_e32 v15, v38
	v_mov_b32_e32 v16, v38
	v_mov_b32_e32 v17, v38
	v_mov_b32_e32 v26, v38
	v_mov_b32_e32 v27, v38
	v_mov_b32_e32 v28, v38
	v_mov_b32_e32 v29, v38
	v_mov_b32_e32 v6, v38
	v_mov_b32_e32 v7, v38
	v_mov_b32_e32 v8, v38
	v_mov_b32_e32 v9, v38
	v_mov_b32_e32 v22, v38
	v_mov_b32_e32 v23, v38
	v_mov_b32_e32 v24, v38
	v_mov_b32_e32 v25, v38
	v_mov_b32_e32 v2, v38
	v_mov_b32_e32 v3, v38
	v_mov_b32_e32 v4, v38
	v_mov_b32_e32 v5, v38
	v_lshl_add_u64 v[32:33], s[6:7], 1, v[70:71]
	v_lshl_add_u64 v[72:73], v[10:11], 1, v[32:33]
	v_lshl_add_u64 v[32:33], v[12:13], 1, v[32:33]
	global_load_dwordx4 v[72:75], v[72:73], off
	s_nop 0
	global_load_dwordx4 v[94:97], v[32:33], off
.LBB0_1718:
	s_add_i32 s6, s6, 32
	v_lshl_add_u64 v[32:33], s[6:7], 1, v[70:71]
	v_lshl_add_u64 v[118:119], v[10:11], 1, v[32:33]
	v_lshl_add_u64 v[32:33], v[12:13], 1, v[32:33]
	global_load_dwordx4 v[110:113], v[118:119], off
	s_nop 0
	global_load_dwordx4 v[114:117], v[32:33], off
	ds_read_b128 v[98:101], v30
	ds_read_b128 v[102:105], v30 offset:37632
	s_waitcnt vmcnt(3) lgkmcnt(1)
	v_mfma_f32_16x16x32_bf16 v[38:41], v[72:75], v[98:101], v[38:41]
	s_waitcnt vmcnt(2)
	v_mfma_f32_16x16x32_bf16 v[18:21], v[94:97], v[98:101], v[18:21]
	ds_read_b128 v[98:101], v30 offset:12544
	ds_read_b128 v[106:109], v30 offset:25088
	v_add_u32_e32 v30, 64, v30
	s_waitcnt lgkmcnt(1)
	v_mfma_f32_16x16x32_bf16 v[34:37], v[72:75], v[98:101], v[34:37]
	v_mfma_f32_16x16x32_bf16 v[14:17], v[94:97], v[98:101], v[14:17]
	s_waitcnt lgkmcnt(0)
	v_mfma_f32_16x16x32_bf16 v[26:29], v[72:75], v[106:109], v[26:29]
	v_mfma_f32_16x16x32_bf16 v[6:9], v[94:97], v[106:109], v[6:9]
	v_mfma_f32_16x16x32_bf16 v[22:25], v[72:75], v[102:105], v[22:25]
	v_mfma_f32_16x16x32_bf16 v[2:5], v[94:97], v[102:105], v[2:5]
	s_add_i32 s0, s0, -2
	s_add_i32 s6, s6, 32
	s_cmp_eq_u32 s0, 0
	s_cbranch_scc1 .Llora_last
	v_lshl_add_u64 v[32:33], s[6:7], 1, v[70:71]
	v_lshl_add_u64 v[72:73], v[10:11], 1, v[32:33]
	v_lshl_add_u64 v[32:33], v[12:13], 1, v[32:33]
	global_load_dwordx4 v[72:75], v[72:73], off
	s_nop 0
	global_load_dwordx4 v[94:97], v[32:33], off
	ds_read_b128 v[98:101], v30
	ds_read_b128 v[102:105], v30 offset:37632
	s_waitcnt vmcnt(3) lgkmcnt(1)
	v_mfma_f32_16x16x32_bf16 v[38:41], v[110:113], v[98:101], v[38:41]
	s_waitcnt vmcnt(2)
	v_mfma_f32_16x16x32_bf16 v[18:21], v[114:117], v[98:101], v[18:21]
	ds_read_b128 v[98:101], v30 offset:12544
	ds_read_b128 v[106:109], v30 offset:25088
	v_add_u32_e32 v30, 64, v30
	s_waitcnt lgkmcnt(1)
	v_mfma_f32_16x16x32_bf16 v[34:37], v[110:113], v[98:101], v[34:37]
	v_mfma_f32_16x16x32_bf16 v[14:17], v[114:117], v[98:101], v[14:17]
	s_waitcnt lgkmcnt(0)
	v_mfma_f32_16x16x32_bf16 v[26:29], v[110:113], v[106:109], v[26:29]
	v_mfma_f32_16x16x32_bf16 v[6:9], v[114:117], v[106:109], v[6:9]
	v_mfma_f32_16x16x32_bf16 v[22:25], v[110:113], v[102:105], v[22:25]
	v_mfma_f32_16x16x32_bf16 v[2:5], v[114:117], v[102:105], v[2:5]
	s_branch .LBB0_1718
.Llora_last:
	ds_read_b128 v[98:101], v30
	ds_read_b128 v[102:105], v30 offset:37632
	s_waitcnt vmcnt(1) lgkmcnt(1)
	v_mfma_f32_16x16x32_bf16 v[38:41], v[110:113], v[98:101], v[38:41]
	s_waitcnt vmcnt(0)
	v_mfma_f32_16x16x32_bf16 v[18:21], v[114:117], v[98:101], v[18:21]
	ds_read_b128 v[98:101], v30 offset:12544
	ds_read_b128 v[106:109], v30 offset:25088
	v_add_u32_e32 v30, 64, v30
	s_waitcnt lgkmcnt(1)
	v_mfma_f32_16x16x32_bf16 v[34:37], v[110:113], v[98:101], v[34:37]
	v_mfma_f32_16x16x32_bf16 v[14:17], v[114:117], v[98:101], v[14:17]
	s_waitcnt lgkmcnt(0)
	v_mfma_f32_16x16x32_bf16 v[26:29], v[110:113], v[106:109], v[26:29]
	v_mfma_f32_16x16x32_bf16 v[6:9], v[114:117], v[106:109], v[6:9]
	v_mfma_f32_16x16x32_bf16 v[22:25], v[110:113], v[102:105], v[22:25]
	v_mfma_f32_16x16x32_bf16 v[2:5], v[114:117], v[102:105], v[2:5]
	v_or_b32_e32 v72, s4, v78
	v_mov_b32_e32 v30, 0
	s_and_b64 vcc, exec, s[18:19]
	v_ashrrev_i32_e32 v73, 31, v72
	v_mov_b32_e32 v31, 0
	v_mov_b32_e32 v32, 0
	v_mov_b32_e32 v33, 0
	s_cbranch_vccnz .LBB0_1771
	s_mov_b64 s[0:1], -1
	s_and_b64 vcc, exec, s[18:19]
	s_cbranch_vccnz .LBB0_1772
